# speedup vs baseline: 1.0265x; 1.0265x over previous
.LBB0_89:
	v_mov_b32_e32 v112, v22
	v_mov_b32_e32 v113, v23
	v_mov_b32_e32 v114, v24
	v_mov_b32_e32 v115, v25
	v_mov_b32_e32 v3, 0
	v_lshlrev_b32_e32 v70, 4, v28
	s_and_saveexec_b64 s[60:61], vcc
	s_cbranch_execz .LBB0_118
	s_mov_b64 s[92:93], s[14:15]
	v_lshl_add_u64 v[22:23], s[12:13], 0, v[2:3]
	s_waitcnt vmcnt(0) lgkmcnt(0)
	v_cndmask_b32_e64 v55, -1, v4, s[0:1]
	s_movk_i32 s0, 0x880
	v_mov_b32_e32 v2, 0x1dd00
	v_mad_u32_u24 v4, v80, s0, v2
	v_lshlrev_b32_e32 v2, 1, v1
	v_mov_b32_e32 v27, v3
	v_mbcnt_hi_u32_b32 v2, -1, v29
	v_lshl_add_u64 v[72:73], v[22:23], 0, v[26:27]
	v_and_b32_e32 v23, 64, v2
	v_xor_b32_e32 v22, 16, v2
	v_add_u32_e32 v23, 64, v23
	v_cmp_lt_i32_e32 vcc, v22, v23
	v_lshlrev_b32_e32 v88, 2, v28
	v_and_b32_e32 v24, 7, v0
	v_cndmask_b32_e32 v22, v2, v22, vcc
	v_lshlrev_b32_e32 v90, 2, v22
	v_xor_b32_e32 v22, 32, v2
	v_cmp_lt_i32_e32 vcc, v22, v23
	s_mov_b32 s24, 0x10000
	v_cndmask_b32_e32 v2, v2, v22, vcc
	v_lshlrev_b32_e32 v91, 2, v2
	v_lshrrev_b32_e32 v2, 2, v79
	v_mul_u32_u24_e32 v22, 0x88, v79
	v_add3_u32 v92, v4, v22, v1
	v_or_b32_e32 v2, v88, v2
	v_lshlrev_b32_e32 v22, 3, v0
	v_mul_u32_u24_e32 v2, 0x88, v2
	v_and_b32_e32 v22, 24, v22
	v_add3_u32 v93, v4, v2, v22
	v_lshlrev_b32_e32 v2, 5, v24
	v_or3_b32 v78, v2, v1, s24
	v_bfe_u32 v2, v0, 1, 2
	v_lshrrev_b32_e32 v89, 3, v79
	v_cmp_eq_u32_e64 s[6:7], 4, v24
	v_cmp_eq_u32_e64 s[8:9], 3, v24
	v_cmp_eq_u32_e64 s[10:11], 2, v24
	v_cmp_eq_u32_e64 s[12:13], 1, v24
	v_cmp_eq_u32_e64 s[14:15], 0, v24
	v_cmp_eq_u32_e64 s[16:17], 7, v24
	v_cmp_eq_u32_e64 s[18:19], 6, v24
	v_cmp_eq_u32_e64 s[20:21], 5, v24
	v_cmp_eq_u32_e64 s[22:23], 0, v2
	v_cmp_eq_u32_e64 s[24:25], 1, v2
	v_cmp_eq_u32_e64 s[26:27], 2, v2
	v_cmp_eq_u32_e64 s[28:29], 3, v2
	s_and_b64 s[22:23], s[22:23], s[4:5]
	s_and_b64 s[24:25], s[24:25], s[4:5]
	s_and_b64 s[26:27], s[26:27], s[4:5]
	s_and_b64 s[28:29], s[28:29], s[4:5]
	v_mov_b32_e32 v71, 0xf149f2ca
	s_mov_b64 s[62:63], 0
	s_mov_b32 s69, 0xf149f2ca
	s_mov_b32 s70, 0xefa18f08
	s_mov_b32 s71, 0x41000000
	s_movk_i32 s72, 0x110
	s_mov_b32 s77, 0x26500
	s_mov_b32 s73, 0x2650c
	s_mov_b32 s80, -1
	s_mov_b32 s81, 0
	s_mov_b32 s82, 0
	s_mov_b32 s83, 0x7fffffff
	s_mov_b64 s[84:85], 0
	v_mov_b32_e32 v100, 0
	v_mov_b32_e32 v4, 0
	v_mov_b32_e32 v103, 0xf149f2ca
	v_mov_b32_e32 v46, v3
	v_mov_b32_e32 v47, v3
	v_mov_b32_e32 v48, v3
	v_mov_b32_e32 v49, v3
	v_mov_b32_e32 v50, v3
	v_mov_b32_e32 v51, v3
	v_mov_b32_e32 v52, v3
	v_mov_b32_e32 v53, v3
	v_mov_b32_e32 v38, v3
	v_mov_b32_e32 v39, v3
	v_mov_b32_e32 v40, v3
	v_mov_b32_e32 v41, v3
	v_mov_b32_e32 v42, v3
	v_mov_b32_e32 v43, v3
	v_mov_b32_e32 v44, v3
	v_mov_b32_e32 v45, v3
	v_mov_b32_e32 v30, v3
	v_mov_b32_e32 v31, v3
	v_mov_b32_e32 v32, v3
	v_mov_b32_e32 v33, v3
	v_mov_b32_e32 v34, v3
	v_mov_b32_e32 v35, v3
	v_mov_b32_e32 v36, v3
	v_mov_b32_e32 v37, v3
	v_mov_b32_e32 v22, v3
	v_mov_b32_e32 v23, v3
	v_mov_b32_e32 v24, v3
	v_mov_b32_e32 v25, v3
	v_mov_b32_e32 v26, v3
	v_mov_b32_e32 v28, v3
	v_mov_b32_e32 v29, v3
	v_readfirstlane_b32 s86, v80
	s_mov_b32 s87, 0
	v_readfirstlane_b32 s88, v99
	v_readfirstlane_b32 s89, v5
	v_readfirstlane_b32 s96, v54
	v_readfirstlane_b32 s97, v84
	v_readfirstlane_b32 s98, v85
	v_readfirstlane_b32 s99, v81
	v_readfirstlane_b32 s100, v83
	v_readfirstlane_b32 s101, v82
	v_mov_b32_e32 v84, v82
	s_cmp_ge_i32 s96, s68
	s_cselect_b32 s100, 0, s100
	s_setprio 1
	s_branch .LBB0_95

.LBB0_118:
	s_or_b64 exec, exec, s[60:61]
	s_setprio 0
	v_readfirstlane_b32 s74, v0
	v_mov_b32_e32 v42, 0
	v_mov_b32_e32 v50, 0
	v_bfe_u32 v36, v0, 6, 2
	v_lshl_or_b32 v44, v36, 13, v86
	v_mov_b32_e32 v45, 0
	v_lshl_add_u64 v[18:19], s[56:57], 0, v[44:45]
	v_add_co_u32_e32 v34, vcc, 0x1000, v18
	global_load_dwordx4 v[2:5], v44, s[56:57]
	global_load_dwordx4 v[6:9], v44, s[56:57] offset:1024
	global_load_dwordx4 v[10:13], v44, s[56:57] offset:2048
	global_load_dwordx4 v[14:17], v44, s[56:57] offset:3072
	v_addc_co_u32_e32 v35, vcc, 0, v19, vcc
	v_lshlrev_b32_e32 v44, 7, v36
	global_load_dwordx4 v[18:21], v[34:35], off
	global_load_dwordx4 v[22:25], v[34:35], off offset:1024
	global_load_dwordx4 v[26:29], v[34:35], off offset:2048
	global_load_dwordx4 v[30:33], v[34:35], off offset:3072
	v_lshl_add_u64 v[34:35], s[52:53], 0, v[44:45]
	v_lshlrev_b32_e32 v36, 2, v1
	v_mov_b32_e32 v37, v45
	v_lshl_add_u64 v[46:47], v[34:35], 0, v[36:37]
	global_load_dwordx4 v[34:37], v[46:47], off offset:16
	global_load_dwordx4 v[38:41], v[46:47], off
	v_add3_u32 v46, s66, v50, v79
	v_ashrrev_i32_e32 v47, 31, v46
	v_and_b32_e32 v0, 48, v0
	v_lshlrev_b64 v[46:47], 9, v[46:47]
	v_lshlrev_b32_e32 v0, 1, v0
	v_or3_b32 v46, v46, v44, v0
	v_mul_u32_u24_e32 v43, 0x110, v79
	s_movk_i32 s0, 0x1100
	v_lshl_add_u64 v[0:1], s[54:55], 0, v[46:47]
	v_mad_u32_u24 v42, v42, s0, v43
	s_mov_b32 s0, 0x10000
	v_lshl_add_u64 v[0:1], v[0:1], 0, 16
	v_add3_u32 v51, v42, v70, s0
	s_lshr_b32 s74, s74, 6
	s_and_b32 s74, s74, 3
	s_lshl_b32 s75, s74, 2
	s_add_i32 s75, s75, 0x26d50
	s_add_i32 s76, s33, 15
	s_lshr_b32 s76, s76, 4
	v_mov_b64_e32 v[60:61], v[0:1]
	v_mov_b32_e32 v62, v51
	s_waitcnt vmcnt(0)
